# speedup vs baseline: 1.0282x; 1.0098x over previous
.LBB1_4:
	s_or_b64 exec, exec, s[4:5]
	v_lshrrev_b32_e32 v6, 3, v0
	v_mul_u32_u24_e32 v4, 48, v0
	v_and_b32_e32 v6, 60, v6
	v_add3_u32 v4, v2, v4, v6
	s_waitcnt lgkmcnt(0)
	s_barrier
	ds_read_b32 v6, v4
	s_load_dwordx4 s[8:11], s[0:1], 0x40
	s_load_dwordx2 s[12:13], s[0:1], 0x28
	ds_read_b32 v2, v3
	v_lshlrev_b32_e64 v15, v0, 1
	s_lshl_b32 s3, s3, 3
	s_waitcnt lgkmcnt(0)
	v_bitop3_b32 v3, v6, v15, v6 bitop3:0x30
	ds_write_b32 v4, v3
	v_cmp_lt_i32_e32 vcc, -1, v2
	s_and_saveexec_b64 s[4:5], vcc
	v_lshlrev_b32_e64 v3, v2, 1
	v_lshrrev_b32_e32 v2, 3, v2
	v_and_b32_e32 v2, 0x1ffffffc, v2
	ds_or_b32 v2, v3 offset:34816
	s_or_b64 exec, exec, s[4:5]
	v_and_b32_e32 v3, 15, v0
	v_add_u32_e32 v8, s3, v1
	v_lshlrev_b32_e32 v4, 2, v3
	v_lshl_or_b32 v2, v8, 6, v4
	s_load_dwordx2 s[16:17], s[0:1], 0x20
	s_waitcnt lgkmcnt(0)
	s_barrier
	ds_read_b32 v6, v2
	s_lshl_b64 s[4:5], s[14:15], 9
	v_mov_b32_e32 v2, v8
	s_waitcnt lgkmcnt(0)
	s_branch .LBB1_8
.LBB1_8:
	v_lshrrev_b32_e32 v7, 5, v2
	v_lshlrev_b32_e64 v9, v2, -2
	v_cmp_eq_u32_e64 s[44:45], v3, v7
	v_cmp_gt_u32_e32 vcc, v3, v7
	v_and_b32_e32 v9, v9, v6
	v_cndmask_b32_e64 v9, 0, v9, s[44:45]
	v_cndmask_b32_e32 v9, v9, v6, vcc
	v_cmp_ne_u32_e32 vcc, 0, v9
	s_and_b32 s3, vcc_lo, 0xffff
	s_cbranch_scc0 .LBB1_13
	s_ff1_i32_b32 s3, s3
	v_readlane_b32 s15, v9, s3
	s_ff1_i32_b32 s15, s15
	s_lshl_b32 s18, s3, 11
	s_lshl_b32 s15, s15, 6
	s_add_i32 s18, s18, s15
	v_lshl_or_b32 v7, v3, 2, s18
	v_cmp_eq_u32_e32 vcc, s3, v3
	v_add_u32_e32 v10, -1, v9
	ds_read_b32 v7, v7
	v_cndmask_b32_e32 v10, -1, v10, vcc
	v_and_b32_e32 v11, v10, v9
	v_cmp_ne_u32_e32 vcc, 0, v11
	s_and_b32 s3, vcc_lo, 0xffff
	s_cbranch_scc0 .Lk2_single
	s_ff1_i32_b32 s3, s3
	v_readlane_b32 s15, v11, s3
	s_ff1_i32_b32 s15, s15
	s_lshl_b32 s20, s3, 5
	s_or_b32 s22, s15, s20
	v_lshl_or_b32 v9, s22, 6, v4
	ds_read_b32 v9, v9
	s_waitcnt lgkmcnt(1)
	v_readlane_b32 s3, v7, s3
	s_lshr_b32 s3, s3, s15
	s_bitcmp0_b32 s3, 0
	s_cselect_b64 vcc, -1, 0
	s_waitcnt lgkmcnt(0)
	v_not_b32_e32 v9, v9
	v_cndmask_b32_e32 v9, -1, v9, vcc
	v_bitop3_b32 v6, v9, v6, v7 bitop3:0x40
	v_mov_b32_e32 v2, s22
	s_branch .LBB1_8
